# phase A StaticOrder::next: row-group size is always 4 (nM=128), so the runtime division by gsz becomes shift/mask (no v_rcp/readfirstlane chain at each unit top); on top of m16
# speedup vs baseline: 1.0045x; 1.0045x over previous
;     DI bool next(int i, Unit& u) const {
;         const long L = (long)i * G + c; if (L >= nwg) return false;
;         int wgid = (int)L; { const int q = nwg / NXCD, r = nwg % NXCD, xcd = wgid % NXCD, off = wgid / NXCD; wgid = (xcd < r ? xcd * (q + 1) : r * (q + 1) + (xcd - r) * q) + off; }
;         const int nig = WGM * nN, gid = wgid / nig, fm = gid * WGM, gsz = (nM - fm) < WGM ? (nM - fm) : WGM;
;         u.pm = fm + ((wgid % nig) % gsz); u.pn = (wgid % nig) / gsz; u.e = 0; u.nv = 256; u.ui = i; return true;
.LBB0_273:
	s_add_i32 s96, s96, 1
	s_mul_i32 s4, s96, s38
	s_mul_hi_u32 s5, s96, s49
	s_add_i32 s5, s5, s4
	s_mul_i32 s4, s96, s49
	s_add_u32 s44, s4, s60
	s_addc_u32 s45, s5, s39
	v_mov_b64_e32 v[6:7], 0x1380
	v_cmp_lt_i64_e64 s[40:41], s[44:45], v[6:7]
	v_mov_b64_e32 v[6:7], 0x137f
	v_cmp_gt_i64_e32 vcc, s[44:45], v[6:7]
	v_mov_b64_e32 v[210:211], 0x10000
	v_mov_b64_e32 v[228:229], 0xffff
	v_mov_b32_e32 v203, 0x3727c5ac
	s_cbranch_vccnz .LBB0_275
	s_ashr_i32 s4, s44, 31
	s_lshr_b32 s4, s4, 29
	s_add_i32 s4, s44, s4
	s_ashr_i32 s5, s4, 3
	s_and_b32 s4, s4, -8
	s_sub_i32 s4, s44, s4
	s_cmp_lt_i32 s4, 0
	s_cselect_b32 s6, s2, 0x270
	s_mul_i32 s4, s4, s6
	s_add_i32 s4, s4, s5
	s_mul_hi_i32 s5, s4, 0xd20d20d3
	s_add_i32 s5, s5, s4
	s_lshr_b32 s6, s5, 31
	s_ashr_i32 s5, s5, 7
	s_add_i32 s5, s5, s6
	s_lshl_b32 s6, s5, 2
	s_sub_i32 s7, 0x80, s6
	s_min_i32 s7, s7, 4
	s_mulk_i32 s5, 0x9c
	s_sub_i32 s4, s4, s5
	s_ashr_i32 s46, s4, 2
	s_and_b32 s4, s4, 3
	s_add_i32 s42, s6, s4
